# P6 activation tile loads nt too
# speedup vs baseline: 1.0017x; 1.0017x over previous
.LBB0_968:
	s_and_b32 s9, s8, 1
	s_ashr_i32 s4, s8, 1
	s_lshl_b32 s56, s9, 9
	s_ashr_i32 s5, s4, 31
	v_lshl_add_u64 v[4:5], v[182:183], 0, s[56:57]
	s_lshl_b64 s[10:11], s[4:5], 19
	v_lshlrev_b64 v[4:5], 9, v[4:5]
	v_lshl_add_u64 v[4:5], v[4:5], 0, s[10:11]
	v_lshl_add_u64 v[6:7], v[184:185], 0, v[4:5]
	global_load_dwordx4 v[36:39], v[6:7], off
	global_load_dwordx4 v[40:43], v[6:7], off offset:32
	global_load_dwordx4 v[44:47], v[6:7], off offset:64
	global_load_dwordx4 v[48:51], v[6:7], off offset:96
	global_load_dwordx4 v[52:55], v[6:7], off offset:128
	global_load_dwordx4 v[56:59], v[6:7], off offset:160
	global_load_dwordx4 v[60:63], v[6:7], off offset:192
	global_load_dwordx4 v[64:67], v[6:7], off offset:224
	global_load_dwordx4 v[68:71], v[6:7], off offset:256
	global_load_dwordx4 v[72:75], v[6:7], off offset:288
	global_load_dwordx4 v[76:79], v[6:7], off offset:320
	global_load_dwordx4 v[80:83], v[6:7], off offset:352
	global_load_dwordx4 v[84:87], v[6:7], off offset:384
	global_load_dwordx4 v[88:91], v[6:7], off offset:416
	global_load_dwordx4 v[92:95], v[6:7], off offset:448
	global_load_dwordx4 v[96:99], v[6:7], off offset:480
	v_or_b32_e32 v4, 0x4000, v4
	v_lshl_add_u64 v[4:5], v[184:185], 0, v[4:5]
	global_load_dwordx4 v[100:103], v[4:5], off
	global_load_dwordx4 v[104:107], v[4:5], off offset:32
	global_load_dwordx4 v[108:111], v[4:5], off offset:64
	global_load_dwordx4 v[112:115], v[4:5], off offset:96
	global_load_dwordx4 v[116:119], v[4:5], off offset:128
	global_load_dwordx4 v[120:123], v[4:5], off offset:160
	global_load_dwordx4 v[124:127], v[4:5], off offset:192
	global_load_dwordx4 v[128:131], v[4:5], off offset:224
	global_load_dwordx4 v[132:135], v[4:5], off offset:256
	global_load_dwordx4 v[136:139], v[4:5], off offset:288
	s_lshl_b32 s10, s4, 8
	s_ashr_i32 s11, s10, 31
	v_lshl_add_u64 v[190:191], s[10:11], 1, v[186:187]
	v_readlane_b32 s10, v253, 42
	v_readlane_b32 s11, v253, 43
	s_andn2_b64 vcc, exec, s[22:23]
	s_nop 0
	v_lshl_add_u64 v[6:7], v[190:191], 0, s[10:11]
	v_readlane_b32 s10, v253, 38
	v_readlane_b32 s11, v253, 39
	s_nop 1
	v_lshl_add_u64 v[8:9], v[190:191], 0, s[10:11]
	global_load_dwordx4 v[156:159], v[6:7], off nt
	global_load_dwordx4 v[168:171], v[8:9], off nt
	v_readlane_b32 s10, v253, 40
	v_readlane_b32 s11, v253, 41
	s_nop 1
	v_lshl_add_u64 v[6:7], v[190:191], 0, s[10:11]
	v_readlane_b32 s10, v253, 44
	v_readlane_b32 s11, v253, 45
	s_nop 1
	v_lshl_add_u64 v[8:9], v[190:191], 0, s[10:11]
	global_load_dwordx4 v[172:175], v[6:7], off nt
	global_load_dwordx4 v[176:179], v[8:9], off nt
	global_load_dwordx4 v[140:143], v[4:5], off offset:320
	global_load_dwordx4 v[144:147], v[4:5], off offset:352
	global_load_dwordx4 v[148:151], v[4:5], off offset:384
	global_load_dwordx4 v[152:155], v[4:5], off offset:416
	global_load_dwordx4 v[160:163], v[4:5], off offset:448
	global_load_dwordx4 v[164:167], v[4:5], off offset:480
	s_waitcnt vmcnt(0)
	s_barrier
	ds_write_b128 v181, v[156:159]
	ds_write_b128 v181, v[168:171] offset:8448
	ds_write_b128 v181, v[172:175] offset:16896
	ds_write_b128 v181, v[176:179] offset:25344
	s_waitcnt lgkmcnt(0)
	s_barrier
	s_cbranch_vccnz .LBB0_967
	s_lshl_b64 s[4:5], s[4:5], 7
	s_lshl_b32 s9, s9, 6
	s_add_u32 s4, s4, s6
	s_addc_u32 s5, s5, s7
	s_add_u32 s4, s4, s9
	s_addc_u32 s5, s5, 0
	s_lshl_b64 s[4:5], s[4:5], 6
	v_mov_b32_e32 v193, s5
	v_or_b32_e32 v192, s4, v180
	s_mov_b32 s9, 0
	s_mov_b32 s4, s21
	s_branch .LBB0_971

.LBB0_971:
	s_add_i32 s12, s4, s20
	s_cmpk_lt_i32 s12, 0x200
	s_cselect_b64 s[14:15], -1, 0
	s_cmpk_gt_i32 s12, 0x1ff
	s_cselect_b64 s[10:11], -1, 0
	s_and_b64 vcc, exec, s[10:11]
	s_cbranch_vccnz .LBB0_973
	s_lshl_b32 s16, s12, 6
	s_ashr_i32 s17, s16, 31
	s_lshl_b64 s[18:19], s[16:17], 11
	v_lshl_add_u64 v[4:5], v[190:191], 0, s[18:19]
	s_or_b32 s18, s16, 16
	s_ashr_i32 s19, s18, 31
	s_lshl_b64 s[18:19], s[18:19], 11
	v_lshl_add_u64 v[6:7], v[190:191], 0, s[18:19]
	s_or_b32 s18, s16, 32
	s_ashr_i32 s19, s18, 31
	s_or_b32 s16, s16, 48
	s_lshl_b64 s[18:19], s[18:19], 11
	s_ashr_i32 s17, s16, 31
	global_load_dwordx4 v[156:159], v[4:5], off nt
	global_load_dwordx4 v[168:171], v[6:7], off nt
	v_lshl_add_u64 v[4:5], v[190:191], 0, s[18:19]
	s_lshl_b64 s[16:17], s[16:17], 11
	v_lshl_add_u64 v[6:7], v[190:191], 0, s[16:17]
	global_load_dwordx4 v[172:175], v[4:5], off nt
	global_load_dwordx4 v[176:179], v[6:7], off nt
